# speedup vs baseline: 1.0007x; 1.0007x over previous
_Z10rnn_kernelPKDF16_S0_PDF16_S1_:
	s_load_dwordx8 s[4:11], s[0:1], 0x0
	v_readfirstlane_b32 s0, v0
	s_lshr_b32 s12, s0, 6
	s_lshl_b32 s0, s12, 4
	s_mov_b32 s1, 0
	s_lshl_b64 s[14:15], s[0:1], 13
	v_and_b32_e32 v1, 63, v0
	s_waitcnt lgkmcnt(0)
	s_add_u32 s6, s6, s14
	s_addc_u32 s7, s7, s15
	v_lshlrev_b32_e32 v142, 4, v1
	v_mov_b32_e32 v143, 0
	v_lshl_add_u64 v[2:3], s[6:7], 0, v[142:143]
	s_movk_i32 s3, 0x1000
	v_add_co_u32_e32 v4, vcc, s3, v2
	s_mov_b32 s13, 0x18000
	s_nop 0
	v_addc_co_u32_e32 v5, vcc, 0, v3, vcc
	v_add_co_u32_e32 v110, vcc, s13, v2
	s_mov_b32 s13, 0x19000
	s_nop 0
	v_addc_co_u32_e32 v111, vcc, 0, v3, vcc
	v_add_co_u32_e32 v50, vcc, s13, v2
	s_mov_b32 s13, 0x1a000
	s_nop 0
	v_addc_co_u32_e32 v51, vcc, 0, v3, vcc
	v_add_co_u32_e32 v52, vcc, s13, v2
	s_movk_i32 s3, 0x2000
	s_nop 0
	v_addc_co_u32_e32 v53, vcc, 0, v3, vcc
	v_add_co_u32_e32 v54, vcc, s3, v2
	s_movk_i32 s3, 0x3000
	s_nop 0
	v_addc_co_u32_e32 v55, vcc, 0, v3, vcc
	global_load_dwordx4 v[6:9], v[110:111], off
	global_load_dwordx4 v[10:13], v[110:111], off offset:1024
	global_load_dwordx4 v[14:17], v[110:111], off offset:2048
	global_load_dwordx4 v[18:21], v[110:111], off offset:3072
	global_load_dwordx4 v[22:25], v[50:51], off offset:1024
	global_load_dwordx4 v[26:29], v[50:51], off offset:2048
	global_load_dwordx4 a[0:3], v[4:5], off offset:1024
	global_load_dwordx4 a[4:7], v[4:5], off offset:2048
	global_load_dwordx4 a[8:11], v[54:55], off offset:-4096
	global_load_dwordx4 a[12:15], v[54:55], off
	global_load_dwordx4 a[16:19], v[54:55], off offset:1024
	global_load_dwordx4 a[20:23], v[54:55], off offset:2048
	global_load_dwordx4 v[30:33], v[50:51], off offset:3072
	global_load_dwordx4 v[34:37], v[52:53], off offset:-4096
	global_load_dwordx4 v[38:41], v[52:53], off
	global_load_dwordx4 v[42:45], v[52:53], off offset:1024
	global_load_dwordx4 v[46:49], v[52:53], off offset:2048
	v_add_co_u32_e32 v50, vcc, s3, v2
	s_movk_i32 s3, 0x4000
	s_nop 0
	v_addc_co_u32_e32 v51, vcc, 0, v3, vcc
	v_add_co_u32_e32 v56, vcc, s3, v2
	s_movk_i32 s3, 0x5000
	s_nop 0
	v_addc_co_u32_e32 v57, vcc, 0, v3, vcc
	global_load_dwordx4 a[24:27], v[54:55], off offset:3072
	global_load_dwordx4 a[28:31], v[56:57], off offset:-4096
	global_load_dwordx4 a[32:35], v[4:5], off offset:3072
	global_load_dwordx4 a[36:39], v[50:51], off offset:1024
	global_load_dwordx4 a[40:43], v[50:51], off offset:2048
	global_load_dwordx4 a[44:47], v[50:51], off offset:3072
	global_load_dwordx4 a[48:51], v[56:57], off
	global_load_dwordx4 a[52:55], v[56:57], off offset:1024
	global_load_dwordx4 a[56:59], v[56:57], off offset:2048
	global_load_dwordx4 a[60:63], v[56:57], off offset:3072
	v_add_co_u32_e32 v4, vcc, s3, v2
	s_movk_i32 s3, 0x6000
	s_nop 0
	v_addc_co_u32_e32 v5, vcc, 0, v3, vcc
	v_add_co_u32_e32 v98, vcc, s3, v2
	s_movk_i32 s3, 0x7000
	s_nop 0
	v_addc_co_u32_e32 v99, vcc, 0, v3, vcc
	v_add_co_u32_e32 v100, vcc, s3, v2
	s_mov_b32 s3, 0x8000
	s_nop 0
	v_addc_co_u32_e32 v101, vcc, 0, v3, vcc
	global_load_dwordx4 v[50:53], v[52:53], off offset:3072
	v_add_co_u32_e32 v102, vcc, s3, v2
	s_mov_b32 s14, 0x1c000
	s_nop 0
	v_addc_co_u32_e32 v103, vcc, 0, v3, vcc
	v_add_co_u32_e32 v82, vcc, s14, v2
	global_load_dwordx4 a[64:67], v[4:5], off offset:1024
	global_load_dwordx4 a[68:71], v[4:5], off offset:2048
	global_load_dwordx4 a[72:75], v[98:99], off offset:-4096
	global_load_dwordx4 a[76:79], v[98:99], off
	global_load_dwordx4 a[80:83], v[98:99], off offset:1024
	global_load_dwordx4 a[84:87], v[98:99], off offset:2048
	v_addc_co_u32_e32 v83, vcc, 0, v3, vcc
	global_load_dwordx4 v[54:57], v[82:83], off offset:-4096
	s_mov_b32 s13, 0x1b000
	v_add_co_u32_e32 v66, vcc, s13, v2
	s_mov_b32 s13, 0x1d000
	s_nop 0
	v_addc_co_u32_e32 v67, vcc, 0, v3, vcc
	global_load_dwordx4 v[58:61], v[66:67], off offset:1024
	global_load_dwordx4 v[62:65], v[66:67], off offset:2048
	s_nop 0
	global_load_dwordx4 v[66:69], v[66:67], off offset:3072
	s_nop 0
	global_load_dwordx4 v[70:73], v[82:83], off
	global_load_dwordx4 v[74:77], v[82:83], off offset:1024
	global_load_dwordx4 v[78:81], v[82:83], off offset:2048
	s_nop 0
	global_load_dwordx4 v[82:85], v[82:83], off offset:3072
	v_add_co_u32_e32 v104, vcc, s13, v2
	s_mov_b32 s13, 0x1e000
	s_nop 0
	v_addc_co_u32_e32 v105, vcc, 0, v3, vcc
	v_add_co_u32_e32 v106, vcc, s13, v2
	s_lshl_b32 s13, s12, 15
	s_nop 0
	v_addc_co_u32_e32 v107, vcc, 0, v3, vcc
	global_load_dwordx4 v[86:89], v[106:107], off offset:-4096
	global_load_dwordx4 v[90:93], v[104:105], off offset:1024
	global_load_dwordx4 v[94:97], v[104:105], off offset:2048
	global_load_dwordx4 a[88:91], v[98:99], off offset:3072
	global_load_dwordx4 a[92:95], v[102:103], off offset:-4096
	global_load_dwordx4 a[96:99], v[4:5], off offset:3072
	global_load_dwordx4 a[100:103], v[100:101], off offset:1024
	global_load_dwordx4 a[104:107], v[100:101], off offset:2048
	global_load_dwordx4 a[108:111], v[100:101], off offset:3072
	global_load_dwordx4 a[112:115], v[102:103], off
	global_load_dwordx4 a[116:119], v[102:103], off offset:1024
	global_load_dwordx4 a[120:123], v[102:103], off offset:2048
	global_load_dwordx4 a[124:127], v[102:103], off offset:3072
	s_add_i32 s13, s13, 0
	v_add_u32_e32 v213, s13, v142
	s_mov_b32 s13, 0x9000
	s_waitcnt vmcnt(54)
	ds_write_b128 v213, v[6:9]
	s_waitcnt vmcnt(53)
	ds_write_b128 v213, v[10:13] offset:1024
	s_waitcnt vmcnt(52)
	ds_write_b128 v213, v[14:17] offset:2048
	s_waitcnt vmcnt(51)
	ds_write_b128 v213, v[18:21] offset:3072
	s_waitcnt vmcnt(41)
	ds_write_b128 v213, v[34:37] offset:4096
	ds_write_b128 v213, v[22:25] offset:5120
	ds_write_b128 v213, v[26:29] offset:6144
	ds_write_b128 v213, v[30:33] offset:7168
	s_waitcnt vmcnt(40)
	ds_write_b128 v213, v[38:41] offset:8192
	s_waitcnt vmcnt(39)
	ds_write_b128 v213, v[42:45] offset:9216
	s_waitcnt vmcnt(38)
	ds_write_b128 v213, v[46:49] offset:10240
	v_add_co_u32_e32 v8, vcc, s13, v2
	s_mov_b32 s13, 0xa000
	s_nop 0
	v_addc_co_u32_e32 v9, vcc, 0, v3, vcc
	v_add_co_u32_e32 v10, vcc, s13, v2
	s_mov_b32 s13, 0xb000
	s_nop 0
	v_addc_co_u32_e32 v11, vcc, 0, v3, vcc
	v_add_co_u32_e32 v12, vcc, s13, v2
	s_mov_b32 s13, 0xc000
	s_nop 0
	v_addc_co_u32_e32 v13, vcc, 0, v3, vcc
	v_and_b32_e32 v32, 15, v0
	v_lshl_or_b32 v206, s2, 4, v32
	v_ashrrev_i32_e32 v207, 31, v206
	v_bfe_u32 v1, v0, 5, 1
	v_lshlrev_b64 v[144:145], 10, v[206:207]
	v_or_b32_e32 v33, s0, v1
	v_bitop3_b32 v1, v1, v32, s0 bitop3:0x36
	s_lshl_b32 s0, s12, 8
	s_mov_b32 s2, 0x400000
	v_bitop3_b32 v153, v33, v32, 12 bitop3:0x36
	v_bitop3_b32 v154, v33, v32, 14 bitop3:0x36
	s_waitcnt vmcnt(27)
	ds_write_b128 v213, v[50:53] offset:11264
	global_load_dwordx4 a[128:131], v[8:9], off offset:1024
	global_load_dwordx4 a[132:135], v[8:9], off offset:2048
	global_load_dwordx4 a[136:139], v[10:11], off offset:-4096
	global_load_dwordx4 a[140:143], v[10:11], off
	global_load_dwordx4 v[4:7], v[104:105], off offset:3072
	global_load_dwordx4 a[144:147], v[10:11], off offset:1024
	global_load_dwordx4 a[148:151], v[10:11], off offset:2048
	global_load_dwordx4 a[152:155], v[8:9], off offset:3072
	global_load_dwordx4 a[156:159], v[12:13], off offset:1024
	global_load_dwordx4 a[160:163], v[12:13], off offset:2048
	global_load_dwordx4 a[164:167], v[12:13], off offset:3072
	v_add_co_u32_e32 v12, vcc, s13, v2
	v_bfe_u32 v218, v0, 4, 2
	s_nop 0
	v_addc_co_u32_e32 v13, vcc, 0, v3, vcc
	global_load_dwordx4 a[168:171], v[10:11], off offset:3072
	global_load_dwordx4 a[172:175], v[12:13], off offset:-4096
	s_waitcnt vmcnt(33)
	ds_write_b128 v213, v[54:57] offset:12288
	global_load_dwordx4 v[8:11], v[106:107], off
	global_load_dwordx4 a[176:179], v[12:13], off
	global_load_dwordx4 a[180:183], v[12:13], off offset:1024
	global_load_dwordx4 a[184:187], v[12:13], off offset:2048
	global_load_dwordx4 a[188:191], v[12:13], off offset:3072
	s_waitcnt vmcnt(37)
	ds_write_b128 v213, v[58:61] offset:13312
	global_load_dwordx4 v[12:15], v[106:107], off offset:1024
	global_load_dwordx4 a[192:195], v142, s[6:7]
	global_load_dwordx4 a[196:199], v142, s[6:7] offset:1024
	global_load_dwordx4 a[200:203], v142, s[6:7] offset:2048
	global_load_dwordx4 a[204:207], v142, s[6:7] offset:3072
	s_mov_b32 s7, 0x1f000
	v_add_co_u32_e32 v16, vcc, s7, v2
	s_waitcnt vmcnt(41)
	ds_write_b128 v213, v[62:65] offset:14336
	global_load_dwordx4 v[24:27], v[106:107], off offset:2048
	s_waitcnt vmcnt(41)
	ds_write_b128 v213, v[66:69] offset:15360
	s_waitcnt vmcnt(40)
	ds_write_b128 v213, v[70:73] offset:16384
	s_waitcnt vmcnt(39)
	ds_write_b128 v213, v[74:77] offset:17408
	s_waitcnt vmcnt(38)
	ds_write_b128 v213, v[78:81] offset:18432
	s_waitcnt vmcnt(37)
	ds_write_b128 v213, v[82:85] offset:19456
	s_waitcnt vmcnt(36)
	ds_write_b128 v213, v[86:89] offset:20480
	s_waitcnt vmcnt(35)
	ds_write_b128 v213, v[90:93] offset:21504
	s_waitcnt vmcnt(34)
	ds_write_b128 v213, v[94:97] offset:22528
	v_addc_co_u32_e32 v17, vcc, 0, v3, vcc
	global_load_dwordx4 v[28:31], v[106:107], off offset:3072
	global_load_dwordx4 v[36:39], v[16:17], off
	global_load_dwordx4 v[40:43], v[16:17], off offset:1024
	global_load_dwordx4 v[48:51], v[16:17], off offset:2048
	global_load_dwordx4 v[52:55], v[16:17], off offset:3072
	v_lshl_add_u64 v[16:17], s[4:5], 0, v[144:145]
	v_lshl_add_u64 v[16:17], v[16:17], 0, s[0:1]
	v_and_b32_e32 v142, 48, v0
	v_lshl_add_u64 v[18:19], v[16:17], 0, v[142:143]
	global_load_dwordx4 v[56:59], v[18:19], off
	s_mov_b32 s1, 0xe000
	v_add_co_u32_e32 v16, vcc, s1, v2
	s_mov_b32 s6, 0xd000
	s_nop 0
	v_addc_co_u32_e32 v17, vcc, 0, v3, vcc
	v_add_co_u32_e32 v20, vcc, s6, v2
	s_mov_b32 s1, 0xf000
	s_nop 0
	v_addc_co_u32_e32 v21, vcc, 0, v3, vcc
	global_load_dwordx4 a[208:211], v[16:17], off offset:-4096
	global_load_dwordx4 a[212:215], v[16:17], off
	global_load_dwordx4 a[216:219], v[16:17], off offset:1024
	global_load_dwordx4 a[220:223], v[16:17], off offset:2048
	global_load_dwordx4 a[224:227], v[20:21], off offset:1024
	global_load_dwordx4 a[228:231], v[20:21], off offset:2048
	v_lshlrev_b32_e32 v143, 10, v32
	v_or_b32_e32 v144, v144, v142
	s_waitcnt vmcnt(31)
	ds_write_b128 v213, v[4:7] offset:23552
	v_add_co_u32_e32 v6, vcc, s1, v2
	s_mov_b32 s1, 0x10000
	s_nop 0
	v_addc_co_u32_e32 v7, vcc, 0, v3, vcc
	v_add_co_u32_e32 v22, vcc, s1, v2
	s_mov_b32 s1, 0x11000
	s_nop 0
	v_addc_co_u32_e32 v23, vcc, 0, v3, vcc
	global_load_dwordx4 a[232:235], v[16:17], off offset:3072
	global_load_dwordx4 a[236:239], v[22:23], off offset:-4096
	global_load_dwordx4 a[240:243], v[20:21], off offset:3072
	global_load_dwordx4 a[244:247], v[6:7], off offset:1024
	s_waitcnt vmcnt(26)
	ds_write_b128 v213, v[8:11] offset:24576
	s_waitcnt vmcnt(21)
	ds_write_b128 v213, v[12:15] offset:25600
	global_load_dwordx4 v[10:13], v[18:19], off offset:64
	v_add_co_u32_e32 v34, vcc, s1, v2
	s_mov_b32 s1, 0x12000
	s_nop 0
	v_addc_co_u32_e32 v35, vcc, 0, v3, vcc
	v_add_co_u32_e32 v66, vcc, s1, v2
	s_mov_b32 s1, 0x13000
	s_nop 0
	v_addc_co_u32_e32 v67, vcc, 0, v3, vcc
	v_add_co_u32_e32 v46, vcc, s1, v2
	s_mov_b32 s1, 0x14000
	s_nop 0
	v_addc_co_u32_e32 v47, vcc, 0, v3, vcc
	v_add_co_u32_e32 v86, vcc, s1, v2
	s_mov_b32 s1, 0x15000
	s_nop 0
	v_addc_co_u32_e32 v87, vcc, 0, v3, vcc
	v_add_co_u32_e32 v122, vcc, s1, v2
	s_mov_b32 s1, 0x16000
	s_nop 0
	v_addc_co_u32_e32 v123, vcc, 0, v3, vcc
	v_lshrrev_b32_e32 v14, 1, v0
	v_add_co_u32_e32 v106, vcc, s1, v2
	v_and_or_b32 v152, v14, 8, v143
	s_waitcnt vmcnt(11)
	v_cvt_f32_f16_e32 v14, v56
	v_addc_co_u32_e32 v107, vcc, 0, v3, vcc
	s_mov_b32 s1, 0x17000
	ds_write_b128 v213, v[24:27] offset:26624
	ds_write_b128 v213, v[28:31] offset:27648
	v_add_co_u32_e32 v134, vcc, s1, v2
	ds_write_b128 v213, v[36:39] offset:28672
	s_nop 0
	v_addc_co_u32_e32 v135, vcc, 0, v3, vcc
	global_load_dwordx4 v[2:5], v[6:7], off offset:2048
	s_nop 0
	global_load_dwordx4 v[6:9], v[6:7], off offset:3072
	ds_write_b128 v213, v[40:43] offset:29696
	ds_write_b128 v213, v[48:51] offset:30720
	ds_write_b128 v213, v[52:55] offset:31744
	v_lshl_add_u32 v217, v1, 4, v152
	v_bitop3_b32 v1, v33, v32, 2 bitop3:0x36
	v_lshl_add_u32 v215, v1, 4, v152
	v_exp_f32_e32 v1, v14
	global_load_dwordx4 v[14:17], v[18:19], off offset:128
	global_load_dwordx4 v[138:141], v[18:19], off offset:192
	v_cvt_f32_f16_sdwa v20, v56 dst_sel:DWORD dst_unused:UNUSED_PAD src0_sel:WORD_1
	v_cvt_f32_f16_e32 v21, v57
	v_cvt_f32_f16_sdwa v25, v57 dst_sel:DWORD dst_unused:UNUSED_PAD src0_sel:WORD_1
	v_add_f32_e32 v1, 1.0, v1
	v_exp_f32_e32 v24, v20
	v_rcp_f32_e32 v20, v1
	v_exp_f32_e32 v1, v21
	v_exp_f32_e32 v25, v25
	v_add_f32_e32 v21, 1.0, v24
	v_rcp_f32_e32 v21, v21
	v_add_f32_e32 v1, 1.0, v1
	v_rcp_f32_e32 v24, v1
	v_add_f32_e32 v1, 1.0, v25
	v_rcp_f32_e32 v25, v1
	v_pk_fma_f32 v[20:21], v[20:21], 2.0, 1.0 op_sel_hi:[1,0,0] neg_lo:[1,0,0] neg_hi:[1,0,0]
	v_cvt_f32_f16_e32 v1, v58
	s_add_i32 s1, 0, 0x24000
	v_pk_fma_f32 v[24:25], v[24:25], 2.0, 1.0 op_sel_hi:[1,0,0] neg_lo:[1,0,0] neg_hi:[1,0,0]
	v_cvt_pk_f16_f32 v20, v20, v21
	v_cvt_pk_f16_f32 v21, v24, v25
	v_add_u32_e32 v24, s1, v217
	ds_write_b64 v24, v[20:21]
	v_cvt_f32_f16_sdwa v20, v58 dst_sel:DWORD dst_unused:UNUSED_PAD src0_sel:WORD_1
	v_exp_f32_e32 v1, v1
	v_cvt_f32_f16_e32 v21, v59
	v_cvt_f32_f16_sdwa v24, v59 dst_sel:DWORD dst_unused:UNUSED_PAD src0_sel:WORD_1
	v_exp_f32_e32 v25, v20
	v_add_f32_e32 v1, 1.0, v1
	v_rcp_f32_e32 v20, v1
	v_exp_f32_e32 v1, v21
	v_add_f32_e32 v21, 1.0, v25
	v_exp_f32_e32 v25, v24
	v_rcp_f32_e32 v21, v21
	v_add_f32_e32 v1, 1.0, v1
	v_rcp_f32_e32 v24, v1
	v_add_f32_e32 v1, 1.0, v25
	v_rcp_f32_e32 v25, v1
	s_waitcnt vmcnt(4)
	v_cvt_f32_f16_e32 v1, v10
	v_cvt_f32_f16_sdwa v10, v10 dst_sel:DWORD dst_unused:UNUSED_PAD src0_sel:WORD_1
	v_pk_fma_f32 v[20:21], v[20:21], 2.0, 1.0 op_sel_hi:[1,0,0] neg_lo:[1,0,0] neg_hi:[1,0,0]
	v_pk_fma_f32 v[24:25], v[24:25], 2.0, 1.0 op_sel_hi:[1,0,0] neg_lo:[1,0,0] neg_hi:[1,0,0]
	v_cvt_pk_f16_f32 v20, v20, v21
	v_cvt_pk_f16_f32 v21, v24, v25
	v_exp_f32_e32 v1, v1
	v_add_u32_e32 v24, s1, v215
	ds_write_b64 v24, v[20:21]
	v_cvt_f32_f16_e32 v20, v11
	v_exp_f32_e32 v21, v10
	v_cvt_f32_f16_sdwa v11, v11 dst_sel:DWORD dst_unused:UNUSED_PAD src0_sel:WORD_1
	v_add_f32_e32 v1, 1.0, v1
	v_rcp_f32_e32 v10, v1
	v_exp_f32_e32 v1, v20
	v_add_f32_e32 v20, 1.0, v21
	v_exp_f32_e32 v21, v11
	v_rcp_f32_e32 v11, v20
	v_add_f32_e32 v1, 1.0, v1
	v_rcp_f32_e32 v20, v1
	v_add_f32_e32 v1, 1.0, v21
	v_rcp_f32_e32 v21, v1
	v_bitop3_b32 v26, v33, v32, 4 bitop3:0x36
	v_bitop3_b32 v1, v33, v32, 6 bitop3:0x36
	v_lshl_add_u32 v211, v26, 4, v152
	v_lshl_add_u32 v212, v1, 4, v152
	v_pk_fma_f32 v[10:11], v[10:11], 2.0, 1.0 op_sel_hi:[1,0,0] neg_lo:[1,0,0] neg_hi:[1,0,0]
	v_pk_fma_f32 v[20:21], v[20:21], 2.0, 1.0 op_sel_hi:[1,0,0] neg_lo:[1,0,0] neg_hi:[1,0,0]
	v_bitop3_b32 v1, v33, v32, 8 bitop3:0x36
	v_cvt_pk_f16_f32 v10, v10, v11
	v_cvt_pk_f16_f32 v11, v20, v21
	v_lshl_add_u32 v210, v1, 4, v152
	v_add_u32_e32 v1, s1, v211
	ds_write_b64 v1, v[10:11]
	v_cvt_f32_f16_e32 v10, v12
	v_cvt_f32_f16_sdwa v11, v12 dst_sel:DWORD dst_unused:UNUSED_PAD src0_sel:WORD_1
	v_cvt_f32_f16_e32 v12, v13
	v_cvt_f32_f16_sdwa v13, v13 dst_sel:DWORD dst_unused:UNUSED_PAD src0_sel:WORD_1
	v_exp_f32_e32 v10, v10
	v_exp_f32_e32 v11, v11
	v_exp_f32_e32 v12, v12
	v_exp_f32_e32 v13, v13
	v_add_f32_e32 v10, 1.0, v10
	v_add_f32_e32 v11, 1.0, v11
	v_add_f32_e32 v12, 1.0, v12
	v_add_f32_e32 v13, 1.0, v13
	v_rcp_f32_e32 v10, v10
	v_rcp_f32_e32 v11, v11
	v_rcp_f32_e32 v12, v12
	v_rcp_f32_e32 v13, v13
	s_waitcnt vmcnt(1)
	v_cvt_f32_f16_e32 v20, v14
	v_pk_fma_f32 v[10:11], v[10:11], 2.0, 1.0 op_sel_hi:[1,0,0] neg_lo:[1,0,0] neg_hi:[1,0,0]
	v_cvt_f32_f16_sdwa v14, v14 dst_sel:DWORD dst_unused:UNUSED_PAD src0_sel:WORD_1
	v_pk_fma_f32 v[12:13], v[12:13], 2.0, 1.0 op_sel_hi:[1,0,0] neg_lo:[1,0,0] neg_hi:[1,0,0]
	v_cvt_pk_f16_f32 v10, v10, v11
	v_cvt_pk_f16_f32 v11, v12, v13
	v_add_u32_e32 v13, s1, v212
	v_exp_f32_e32 v12, v20
	ds_write_b64 v13, v[10:11]
	v_cvt_f32_f16_e32 v11, v15
	v_cvt_f32_f16_sdwa v13, v15 dst_sel:DWORD dst_unused:UNUSED_PAD src0_sel:WORD_1
	v_add_f32_e32 v10, 1.0, v12
	v_exp_f32_e32 v12, v14
	v_exp_f32_e32 v14, v11
	v_exp_f32_e32 v13, v13
	v_rcp_f32_e32 v10, v10
	v_add_f32_e32 v11, 1.0, v12
	v_add_f32_e32 v12, 1.0, v14
	v_add_f32_e32 v13, 1.0, v13
	v_rcp_f32_e32 v11, v11
	v_rcp_f32_e32 v12, v12
	v_rcp_f32_e32 v13, v13
	v_cvt_f32_f16_e32 v14, v16
	v_pk_fma_f32 v[10:11], v[10:11], 2.0, 1.0 op_sel_hi:[1,0,0] neg_lo:[1,0,0] neg_hi:[1,0,0]
	v_add_co_u32_e32 v150, vcc, s2, v18
	v_pk_fma_f32 v[12:13], v[12:13], 2.0, 1.0 op_sel_hi:[1,0,0] neg_lo:[1,0,0] neg_hi:[1,0,0]
	v_cvt_pk_f16_f32 v10, v10, v11
	v_cvt_pk_f16_f32 v11, v12, v13
	v_exp_f32_e32 v12, v14
	v_cvt_f32_f16_sdwa v14, v16 dst_sel:DWORD dst_unused:UNUSED_PAD src0_sel:WORD_1
	v_add_u32_e32 v13, s1, v210
	ds_write_b64 v13, v[10:11]
	v_add_f32_e32 v10, 1.0, v12
	v_cvt_f32_f16_e32 v11, v17
	v_exp_f32_e32 v12, v14
	v_cvt_f32_f16_sdwa v13, v17 dst_sel:DWORD dst_unused:UNUSED_PAD src0_sel:WORD_1
	v_rcp_f32_e32 v10, v10
	v_exp_f32_e32 v14, v11
	v_add_f32_e32 v11, 1.0, v12
	v_exp_f32_e32 v12, v13
	v_rcp_f32_e32 v11, v11
	v_add_f32_e32 v13, 1.0, v14
	v_bitop3_b32 v1, v33, v32, 10 bitop3:0x36
	v_add_f32_e32 v12, 1.0, v12
	v_rcp_f32_e32 v146, v13
	v_rcp_f32_e32 v147, v12
	v_pk_fma_f32 v[148:149], v[10:11], 2.0, 1.0 op_sel_hi:[1,0,0] neg_lo:[1,0,0] neg_hi:[1,0,0]
	global_load_dwordx4 v[10:13], v[22:23], off
	global_load_dwordx4 v[14:17], v[22:23], off offset:1024
	v_addc_co_u32_e32 v151, vcc, 0, v19, vcc
	global_load_dwordx4 v[18:21], v[22:23], off offset:2048
	s_nop 0
	global_load_dwordx4 v[22:25], v[22:23], off offset:3072
	s_nop 0
	global_load_dwordx4 v[26:29], v[34:35], off offset:1024
	global_load_dwordx4 v[30:33], v[34:35], off offset:2048
	s_nop 0
	global_load_dwordx4 v[34:37], v[34:35], off offset:3072
	s_nop 0
	global_load_dwordx4 v[38:41], v[46:47], off offset:1024
	global_load_dwordx4 v[42:45], v[46:47], off offset:2048
	s_nop 0
	global_load_dwordx4 v[46:49], v[46:47], off offset:3072
	s_nop 0
	global_load_dwordx4 v[50:53], v[66:67], off offset:-4096
	global_load_dwordx4 v[54:57], v[66:67], off
	global_load_dwordx4 v[58:61], v[66:67], off offset:1024
	global_load_dwordx4 v[62:65], v[66:67], off offset:2048
	s_nop 0
	global_load_dwordx4 v[66:69], v[66:67], off offset:3072
	s_nop 0
	global_load_dwordx4 v[70:73], v[86:87], off offset:-4096
	global_load_dwordx4 v[74:77], v[86:87], off
	global_load_dwordx4 v[78:81], v[86:87], off offset:1024
	global_load_dwordx4 v[82:85], v[86:87], off offset:2048
	s_nop 0
	global_load_dwordx4 v[86:89], v[86:87], off offset:3072
	s_nop 0
	global_load_dwordx4 v[90:93], v[106:107], off offset:-4096
	global_load_dwordx4 v[94:97], v[106:107], off
	global_load_dwordx4 v[98:101], v[106:107], off offset:1024
	global_load_dwordx4 v[102:105], v[106:107], off offset:2048
	s_nop 0
	global_load_dwordx4 v[106:109], v[106:107], off offset:3072
	s_nop 0
	global_load_dwordx4 v[110:113], v[110:111], off offset:-4096
	s_nop 0
	global_load_dwordx4 v[114:117], v[122:123], off offset:1024
	global_load_dwordx4 v[118:121], v[122:123], off offset:2048
	s_nop 0
	global_load_dwordx4 v[122:125], v[122:123], off offset:3072
	s_nop 0
	global_load_dwordx4 v[126:129], v[134:135], off offset:1024
	global_load_dwordx4 v[130:133], v[134:135], off offset:2048
	s_nop 0
	global_load_dwordx4 v[134:137], v[134:135], off offset:3072
	s_nop 0
	global_load_dwordx4 v[178:181], v[150:151], off
	global_load_dwordx4 v[174:177], v[150:151], off offset:64
	global_load_dwordx4 v[170:173], v[150:151], off offset:128
	global_load_dwordx4 v[202:205], v[150:151], off offset:192
	s_waitcnt vmcnt(36)
	v_cvt_f32_f16_e32 v155, v138
	v_cvt_f32_f16_sdwa v138, v138 dst_sel:DWORD dst_unused:UNUSED_PAD src0_sel:WORD_1
	v_pk_fma_f32 v[146:147], v[146:147], 2.0, 1.0 op_sel_hi:[1,0,0] neg_lo:[1,0,0] neg_hi:[1,0,0]
	v_cvt_pk_f16_f32 v148, v148, v149
	v_exp_f32_e32 v150, v155
	v_cvt_pk_f16_f32 v149, v146, v147
	v_cvt_f32_f16_e32 v147, v139
	v_cvt_f32_f16_sdwa v139, v139 dst_sel:DWORD dst_unused:UNUSED_PAD src0_sel:WORD_1
	v_add_f32_e32 v146, 1.0, v150
	v_exp_f32_e32 v150, v138
	v_rcp_f32_e32 v138, v146
	v_exp_f32_e32 v146, v147
	v_lshl_add_u32 v1, v1, 4, v152
	v_add_f32_e32 v147, 1.0, v150
	v_exp_f32_e32 v150, v139
	v_rcp_f32_e32 v139, v147
	v_add_f32_e32 v146, 1.0, v146
	v_rcp_f32_e32 v146, v146
	v_add_f32_e32 v147, 1.0, v150
	v_rcp_f32_e32 v147, v147
	v_pk_fma_f32 v[138:139], v[138:139], 2.0, 1.0 op_sel_hi:[1,0,0] neg_lo:[1,0,0] neg_hi:[1,0,0]
	v_add_u32_e32 v151, s1, v1
	v_cvt_pk_f16_f32 v138, v138, v139
	v_pk_fma_f32 v[146:147], v[146:147], 2.0, 1.0 op_sel_hi:[1,0,0] neg_lo:[1,0,0] neg_hi:[1,0,0]
	ds_write_b64 v151, v[148:149]
	v_cvt_pk_f16_f32 v139, v146, v147
	v_cvt_f32_f16_e32 v146, v140
	v_cvt_f32_f16_sdwa v140, v140 dst_sel:DWORD dst_unused:UNUSED_PAD src0_sel:WORD_1
	v_cvt_f32_f16_e32 v147, v141
	v_cvt_f32_f16_sdwa v141, v141 dst_sel:DWORD dst_unused:UNUSED_PAD src0_sel:WORD_1
	v_exp_f32_e32 v146, v146
	v_exp_f32_e32 v148, v140
	v_lshl_add_u32 v216, v153, 4, v152
	v_lshl_add_u32 v214, v154, 4, v152
	v_add_f32_e32 v140, 1.0, v146
	v_exp_f32_e32 v146, v147
	v_add_f32_e32 v147, 1.0, v148
	v_exp_f32_e32 v148, v141
	v_rcp_f32_e32 v141, v147
	v_add_f32_e32 v146, 1.0, v146
	v_rcp_f32_e32 v140, v140
	v_add_f32_e32 v147, 1.0, v148
	v_rcp_f32_e32 v146, v146
	v_rcp_f32_e32 v147, v147
	v_add_u32_e32 v148, s1, v216
	ds_write_b64 v148, v[138:139]
	v_pk_fma_f32 v[138:139], v[140:141], 2.0, 1.0 op_sel_hi:[1,0,0] neg_lo:[1,0,0] neg_hi:[1,0,0]
	v_pk_fma_f32 v[140:141], v[146:147], 2.0, 1.0 op_sel_hi:[1,0,0] neg_lo:[1,0,0] neg_hi:[1,0,0]
	v_cvt_pk_f16_f32 v138, v138, v139
	v_cvt_pk_f16_f32 v139, v140, v141
	v_add_u32_e32 v140, s1, v214
	s_lshl_b32 s2, s12, 7
	s_add_i32 s1, 0, 0x20000
	s_add_u32 s0, s4, s0
	ds_write_b64 v140, v[138:139]
	v_add_u32_e32 v219, s1, v143
	v_bitop3_b32 v138, v218, v0, 15 bitop3:0x78
	s_addc_u32 s1, s5, 0
	v_lshlrev_b32_e32 v220, 4, v138
	v_lshl_add_u64 v[138:139], s[0:1], 0, v[144:145]
	s_mov_b64 s[0:1], 0x800080
	s_waitcnt lgkmcnt(0)
	s_barrier
	v_lshl_add_u64 v[208:209], v[138:139], 0, s[0:1]
	s_waitcnt vmcnt(0)
	v_mov_b32_e32 v232, v170
	v_mov_b32_e32 v233, v171
	v_mov_b32_e32 v234, v172
	v_mov_b32_e32 v235, v173
	v_mov_b32_e32 v236, v202
	v_mov_b32_e32 v237, v203
	v_mov_b32_e32 v238, v204
	v_mov_b32_e32 v239, v205
	v_cvt_f32_f16_e32 v198, v178
	v_cvt_f32_f16_sdwa v199, v178 dst_sel:DWORD dst_unused:UNUSED_PAD src0_sel:WORD_1
	v_cvt_f32_f16_e32 v200, v179
	v_cvt_f32_f16_sdwa v201, v179 dst_sel:DWORD dst_unused:UNUSED_PAD src0_sel:WORD_1
	v_cvt_f32_f16_e32 v194, v180
	v_cvt_f32_f16_sdwa v195, v180 dst_sel:DWORD dst_unused:UNUSED_PAD src0_sel:WORD_1
	v_cvt_f32_f16_e32 v196, v181
	v_cvt_f32_f16_sdwa v197, v181 dst_sel:DWORD dst_unused:UNUSED_PAD src0_sel:WORD_1
	v_cvt_f32_f16_e32 v190, v174
	v_cvt_f32_f16_sdwa v191, v174 dst_sel:DWORD dst_unused:UNUSED_PAD src0_sel:WORD_1
	v_cvt_f32_f16_e32 v192, v175
	v_cvt_f32_f16_sdwa v193, v175 dst_sel:DWORD dst_unused:UNUSED_PAD src0_sel:WORD_1
	v_cvt_f32_f16_e32 v186, v176
	v_cvt_f32_f16_sdwa v187, v176 dst_sel:DWORD dst_unused:UNUSED_PAD src0_sel:WORD_1
	v_cvt_f32_f16_e32 v188, v177
	v_cvt_f32_f16_sdwa v189, v177 dst_sel:DWORD dst_unused:UNUSED_PAD src0_sel:WORD_1
	s_mov_b32 s6, 0xff800000
	s_mov_b32 s7, -1
	v_lshl_add_u64 v[240:241], v[208:209], 0, s[6:7]
	global_load_dwordx4 v[244:247], v[240:241], off
	global_load_dwordx4 v[202:205], v[240:241], off offset:64
	s_mov_b64 s[0:1], 0x400000
	v_xor_b32_e32 v221, 64, v220
	v_xor_b32_e32 v222, 0x80, v220
	v_xor_b32_e32 v223, 0xc0, v220
	ds_read_b128 v[154:157], v213 offset:0
	ds_read_b128 v[158:161], v213 offset:1024
	ds_read_b128 v[162:165], v213 offset:2048
	ds_read_b128 v[166:169], v213 offset:3072
	s_waitcnt vmcnt(0)
	v_cvt_f32_f16_e32 v182, v244
	v_cvt_f32_f16_sdwa v183, v244 dst_sel:DWORD dst_unused:UNUSED_PAD src0_sel:WORD_1
	v_cvt_f32_f16_e32 v184, v245
	v_cvt_f32_f16_sdwa v185, v245 dst_sel:DWORD dst_unused:UNUSED_PAD src0_sel:WORD_1
	v_cvt_f32_f16_e32 v178, v246
	v_cvt_f32_f16_sdwa v179, v246 dst_sel:DWORD dst_unused:UNUSED_PAD src0_sel:WORD_1
	v_cvt_f32_f16_e32 v180, v247
	v_cvt_f32_f16_sdwa v181, v247 dst_sel:DWORD dst_unused:UNUSED_PAD src0_sel:WORD_1
	v_cvt_f32_f16_e32 v174, v202
	v_cvt_f32_f16_sdwa v175, v202 dst_sel:DWORD dst_unused:UNUSED_PAD src0_sel:WORD_1
	v_cvt_f32_f16_e32 v176, v203
	v_cvt_f32_f16_sdwa v177, v203 dst_sel:DWORD dst_unused:UNUSED_PAD src0_sel:WORD_1
	v_cvt_f32_f16_e32 v170, v204
	v_cvt_f32_f16_sdwa v171, v204 dst_sel:DWORD dst_unused:UNUSED_PAD src0_sel:WORD_1
	v_cvt_f32_f16_e32 v172, v205
	v_cvt_f32_f16_sdwa v173, v205 dst_sel:DWORD dst_unused:UNUSED_PAD src0_sel:WORD_1
	s_waitcnt lgkmcnt(0)
.Lrnn_top:
	s_add_i32 s4, s3, 0xffffc000
	s_and_b32 s4, s4, 0x4000
	s_and_b32 s5, s3, 0x4000
	s_add_i32 s5, s5, 0x20000
	s_add_i32 s6, s4, 0x20000
	v_add_u32_e32 v244, s4, v219
	v_add_u32_e32 v240, v244, v220
	v_add_u32_e32 v241, v244, v221
	v_add_u32_e32 v242, v244, v222
	v_add_u32_e32 v243, v244, v223
	ds_read_b128 v[138:141], v240 offset:0
	ds_read_b128 v[142:145], v241 offset:0
	ds_read_b128 v[146:149], v240 offset:256
	ds_read_b128 v[150:153], v240 offset:768
	s_cmp_eq_u32 s3, 0x40000
	s_cbranch_scc1 .Lrnn_sk1
	global_load_dwordx4 v[224:227], v[208:209], off offset:-128
	global_load_dwordx4 v[228:231], v[208:209], off offset:-64
.Lrnn_sk1:
	v_exp_f32_e32 v182, v182
	v_exp_f32_e32 v183, v183
	v_exp_f32_e32 v184, v184
	v_exp_f32_e32 v185, v185
	v_exp_f32_e32 v178, v178
	v_exp_f32_e32 v179, v179
	v_exp_f32_e32 v180, v180
	v_exp_f32_e32 v181, v181
	v_exp_f32_e32 v174, v174
	v_exp_f32_e32 v175, v175
	v_exp_f32_e32 v176, v176
	v_exp_f32_e32 v177, v177
	s_waitcnt lgkmcnt(3)
	v_mfma_f32_16x16x32_f16 v[198:201], a[192:195], v[138:141], v[198:201]
	v_exp_f32_e32 v170, v170
	v_exp_f32_e32 v171, v171
	v_mfma_f32_16x16x32_f16 v[194:197], a[196:199], v[138:141], v[194:197]
	v_exp_f32_e32 v172, v172
	v_exp_f32_e32 v173, v173
	v_mfma_f32_16x16x32_f16 v[190:193], a[200:203], v[138:141], v[190:193]
	v_add_f32_e32 v182, 1.0, v182
	v_add_f32_e32 v183, 1.0, v183
	v_add_f32_e32 v184, 1.0, v184
	v_add_f32_e32 v185, 1.0, v185
	v_mfma_f32_16x16x32_f16 v[186:189], a[204:207], v[138:141], v[186:189]
	ds_read_b128 v[138:141], v241 offset:256
	v_add_f32_e32 v178, 1.0, v178
	v_add_f32_e32 v179, 1.0, v179
	v_add_f32_e32 v180, 1.0, v180
	v_add_f32_e32 v181, 1.0, v181
	s_waitcnt lgkmcnt(3)
	v_mfma_f32_16x16x32_f16 v[198:201], a[12:15], v[142:145], v[198:201]
	v_add_f32_e32 v174, 1.0, v174
	v_add_f32_e32 v175, 1.0, v175
	v_add_f32_e32 v176, 1.0, v176
	v_add_f32_e32 v177, 1.0, v177
	v_mfma_f32_16x16x32_f16 v[194:197], a[16:19], v[142:145], v[194:197]
	v_add_f32_e32 v170, 1.0, v170
	v_add_f32_e32 v171, 1.0, v171
	v_add_f32_e32 v172, 1.0, v172
	v_add_f32_e32 v173, 1.0, v173
	v_mfma_f32_16x16x32_f16 v[190:193], a[20:23], v[142:145], v[190:193]
	v_rcp_f32_e32 v182, v182
	v_rcp_f32_e32 v183, v183
	v_mfma_f32_16x16x32_f16 v[186:189], a[24:27], v[142:145], v[186:189]
	ds_read_b128 v[142:145], v240 offset:512
	v_rcp_f32_e32 v184, v184
	v_rcp_f32_e32 v185, v185
	s_waitcnt lgkmcnt(3)
	v_mfma_f32_16x16x32_f16 v[198:201], a[112:115], v[146:149], v[198:201]
	v_rcp_f32_e32 v178, v178
	v_rcp_f32_e32 v179, v179
	v_mfma_f32_16x16x32_f16 v[194:197], a[116:119], v[146:149], v[194:197]
	v_rcp_f32_e32 v180, v180
	v_rcp_f32_e32 v181, v181
	v_mfma_f32_16x16x32_f16 v[190:193], a[120:123], v[146:149], v[190:193]
	v_rcp_f32_e32 v174, v174
	v_rcp_f32_e32 v175, v175
	v_mfma_f32_16x16x32_f16 v[186:189], a[124:127], v[146:149], v[186:189]
	ds_read_b128 v[146:149], v241 offset:512
	v_rcp_f32_e32 v176, v176
	v_rcp_f32_e32 v177, v177
	s_waitcnt lgkmcnt(3)
	v_mfma_f32_16x16x32_f16 v[198:201], v[154:157], v[150:153], v[198:201]
	ds_read_b128 v[154:157], v213 offset:8192
	v_rcp_f32_e32 v170, v170
	v_rcp_f32_e32 v171, v171
	v_mfma_f32_16x16x32_f16 v[194:197], v[158:161], v[150:153], v[194:197]
	ds_read_b128 v[158:161], v213 offset:9216
	v_rcp_f32_e32 v172, v172
	v_rcp_f32_e32 v173, v173
	v_mfma_f32_16x16x32_f16 v[190:193], v[162:165], v[150:153], v[190:193]
	ds_read_b128 v[162:165], v213 offset:10240
	v_fma_f32 v182, v182, -2.0, 1.0
	v_fma_f32 v183, v183, -2.0, 1.0
	v_fma_f32 v184, v184, -2.0, 1.0
	v_fma_f32 v185, v185, -2.0, 1.0
	v_mfma_f32_16x16x32_f16 v[186:189], v[166:169], v[150:153], v[186:189]
	ds_read_b128 v[166:169], v213 offset:11264
	ds_read_b128 v[150:153], v241 offset:768
	v_fma_f32 v178, v178, -2.0, 1.0
	v_fma_f32 v179, v179, -2.0, 1.0
	v_fma_f32 v180, v180, -2.0, 1.0
	v_fma_f32 v181, v181, -2.0, 1.0
	s_waitcnt lgkmcnt(7)
	v_mfma_f32_16x16x32_f16 v[198:201], a[140:143], v[138:141], v[198:201]
	v_fma_f32 v174, v174, -2.0, 1.0
	v_fma_f32 v175, v175, -2.0, 1.0
	v_fma_f32 v176, v176, -2.0, 1.0
	v_fma_f32 v177, v177, -2.0, 1.0
	v_mfma_f32_16x16x32_f16 v[194:197], a[144:147], v[138:141], v[194:197]
	v_fma_f32 v170, v170, -2.0, 1.0
	v_fma_f32 v171, v171, -2.0, 1.0
	v_fma_f32 v172, v172, -2.0, 1.0
	v_fma_f32 v173, v173, -2.0, 1.0
	v_mfma_f32_16x16x32_f16 v[190:193], a[148:151], v[138:141], v[190:193]
	v_cvt_pk_f16_f32 v182, v182, v183
	v_cvt_pk_f16_f32 v183, v184, v185
	v_cvt_pk_f16_f32 v178, v178, v179
	v_cvt_pk_f16_f32 v179, v180, v181
	v_mfma_f32_16x16x32_f16 v[186:189], a[168:171], v[138:141], v[186:189]
	v_cvt_pk_f16_f32 v174, v174, v175
	v_cvt_pk_f16_f32 v175, v176, v177
	v_cvt_pk_f16_f32 v170, v170, v171
	v_cvt_pk_f16_f32 v171, v172, v173
	s_waitcnt lgkmcnt(6)
	v_mfma_f32_16x16x32_f16 v[198:201], v[10:13], v[142:145], v[198:201]
	v_add_u32_e32 v202, s6, v210
	ds_write_b64 v202, v[182:183]
	v_add_u32_e32 v203, s6, v1
	v_mfma_f32_16x16x32_f16 v[194:197], v[14:17], v[142:145], v[194:197]
	ds_write_b64 v203, v[178:179]
	v_add_u32_e32 v204, s6, v216
	v_mfma_f32_16x16x32_f16 v[190:193], v[18:21], v[142:145], v[190:193]
	ds_write_b64 v204, v[174:175]
	v_add_u32_e32 v205, s6, v214
	v_mfma_f32_16x16x32_f16 v[186:189], v[22:25], v[142:145], v[186:189]
	ds_write_b64 v205, v[170:171]
	s_waitcnt lgkmcnt(0)
	s_barrier
	ds_read_b128 v[138:141], v242 offset:0
	ds_read_b128 v[142:145], v243 offset:0
	v_mfma_f32_16x16x32_f16 v[198:201], v[54:57], v[146:149], v[198:201]
	s_waitcnt vmcnt(2)
	v_cvt_f32_f16_e32 v182, v232
	v_mfma_f32_16x16x32_f16 v[194:197], v[58:61], v[146:149], v[194:197]
	v_cvt_f32_f16_sdwa v183, v232 dst_sel:DWORD dst_unused:UNUSED_PAD src0_sel:WORD_1
	v_cvt_f32_f16_e32 v184, v233
	v_mfma_f32_16x16x32_f16 v[190:193], v[62:65], v[146:149], v[190:193]
	v_cvt_f32_f16_sdwa v185, v233 dst_sel:DWORD dst_unused:UNUSED_PAD src0_sel:WORD_1
	v_cvt_f32_f16_e32 v178, v234
	v_mfma_f32_16x16x32_f16 v[186:189], v[66:69], v[146:149], v[186:189]
	ds_read_b128 v[146:149], v242 offset:256
	v_cvt_f32_f16_sdwa v179, v234 dst_sel:DWORD dst_unused:UNUSED_PAD src0_sel:WORD_1
	v_cvt_f32_f16_e32 v180, v235
	v_mfma_f32_16x16x32_f16 v[198:201], v[154:157], v[150:153], v[198:201]
	ds_read_b128 v[154:157], v213 offset:16384
	v_cvt_f32_f16_sdwa v181, v235 dst_sel:DWORD dst_unused:UNUSED_PAD src0_sel:WORD_1
	v_cvt_f32_f16_e32 v174, v236
	v_mfma_f32_16x16x32_f16 v[194:197], v[158:161], v[150:153], v[194:197]
	ds_read_b128 v[158:161], v213 offset:17408
	v_cvt_f32_f16_sdwa v175, v236 dst_sel:DWORD dst_unused:UNUSED_PAD src0_sel:WORD_1
	v_cvt_f32_f16_e32 v176, v237
	v_mfma_f32_16x16x32_f16 v[190:193], v[162:165], v[150:153], v[190:193]
	ds_read_b128 v[162:165], v213 offset:18432
	v_cvt_f32_f16_sdwa v177, v237 dst_sel:DWORD dst_unused:UNUSED_PAD src0_sel:WORD_1
	v_cvt_f32_f16_e32 v170, v238
	v_mfma_f32_16x16x32_f16 v[186:189], v[166:169], v[150:153], v[186:189]
	ds_read_b128 v[166:169], v213 offset:19456
	ds_read_b128 v[150:153], v242 offset:768
	v_cvt_f32_f16_sdwa v171, v238 dst_sel:DWORD dst_unused:UNUSED_PAD src0_sel:WORD_1
	v_cvt_f32_f16_e32 v172, v239
	s_waitcnt lgkmcnt(7)
	v_mfma_f32_16x16x32_f16 v[198:201], a[48:51], v[138:141], v[198:201]
	v_cvt_f32_f16_sdwa v173, v239 dst_sel:DWORD dst_unused:UNUSED_PAD src0_sel:WORD_1
	v_mfma_f32_16x16x32_f16 v[194:197], a[52:55], v[138:141], v[194:197]
	s_cmp_eq_u32 s3, 0x40000
	s_cbranch_scc1 .Lrnn_sk2
	global_load_dwordx4 v[232:235], v[208:209], off
	global_load_dwordx4 v[236:239], v[208:209], off offset:64
.Lrnn_sk2:
	v_mfma_f32_16x16x32_f16 v[190:193], a[56:59], v[138:141], v[190:193]
	v_mfma_f32_16x16x32_f16 v[186:189], a[60:63], v[138:141], v[186:189]
	ds_read_b128 v[138:141], v243 offset:256
	s_waitcnt lgkmcnt(7)
	v_mfma_f32_16x16x32_f16 v[198:201], a[76:79], v[142:145], v[198:201]
	v_mfma_f32_16x16x32_f16 v[194:197], a[80:83], v[142:145], v[194:197]
	v_mfma_f32_16x16x32_f16 v[190:193], a[84:87], v[142:145], v[190:193]
	v_mfma_f32_16x16x32_f16 v[186:189], a[88:91], v[142:145], v[186:189]
	ds_read_b128 v[142:145], v242 offset:512
	s_waitcnt lgkmcnt(7)
	v_mfma_f32_16x16x32_f16 v[198:201], a[176:179], v[146:149], v[198:201]
	v_mfma_f32_16x16x32_f16 v[194:197], a[180:183], v[146:149], v[194:197]
	v_mfma_f32_16x16x32_f16 v[190:193], a[184:187], v[146:149], v[190:193]
	v_mfma_f32_16x16x32_f16 v[186:189], a[188:191], v[146:149], v[186:189]
	ds_read_b128 v[146:149], v243 offset:512
	s_waitcnt lgkmcnt(3)
	v_mfma_f32_16x16x32_f16 v[198:201], v[154:157], v[150:153], v[198:201]
	ds_read_b128 v[154:157], v213 offset:24576
	v_mfma_f32_16x16x32_f16 v[194:197], v[158:161], v[150:153], v[194:197]
	ds_read_b128 v[158:161], v213 offset:25600
	v_mfma_f32_16x16x32_f16 v[190:193], v[162:165], v[150:153], v[190:193]
	ds_read_b128 v[162:165], v213 offset:26624
	v_mfma_f32_16x16x32_f16 v[186:189], v[166:169], v[150:153], v[186:189]
	ds_read_b128 v[166:169], v213 offset:27648
	ds_read_b128 v[150:153], v243 offset:768
	s_waitcnt lgkmcnt(7)
	v_mfma_f32_16x16x32_f16 v[198:201], a[212:215], v[138:141], v[198:201]
	v_mfma_f32_16x16x32_f16 v[194:197], a[216:219], v[138:141], v[194:197]
	v_mfma_f32_16x16x32_f16 v[190:193], a[220:223], v[138:141], v[190:193]
	v_mfma_f32_16x16x32_f16 v[186:189], a[232:235], v[138:141], v[186:189]
	ds_read_b128 v[138:141], v240 offset:0
	s_waitcnt lgkmcnt(7)
	v_mfma_f32_16x16x32_f16 v[198:201], v[74:77], v[142:145], v[198:201]
	v_mfma_f32_16x16x32_f16 v[194:197], v[78:81], v[142:145], v[194:197]
	v_mfma_f32_16x16x32_f16 v[190:193], v[82:85], v[142:145], v[190:193]
	v_mfma_f32_16x16x32_f16 v[186:189], v[86:89], v[142:145], v[186:189]
	ds_read_b128 v[142:145], v241 offset:0
	s_waitcnt lgkmcnt(7)
	v_mfma_f32_16x16x32_f16 v[198:201], v[94:97], v[146:149], v[198:201]
	v_mfma_f32_16x16x32_f16 v[194:197], v[98:101], v[146:149], v[194:197]
	v_mfma_f32_16x16x32_f16 v[190:193], v[102:105], v[146:149], v[190:193]
	v_mfma_f32_16x16x32_f16 v[186:189], v[106:109], v[146:149], v[186:189]
	ds_read_b128 v[146:149], v240 offset:256
	s_waitcnt lgkmcnt(3)
	v_mfma_f32_16x16x32_f16 v[198:201], v[154:157], v[150:153], v[198:201]
	ds_read_b128 v[154:157], v213 offset:4096
	v_mfma_f32_16x16x32_f16 v[194:197], v[158:161], v[150:153], v[194:197]
	ds_read_b128 v[158:161], v213 offset:5120
	v_mfma_f32_16x16x32_f16 v[190:193], v[162:165], v[150:153], v[190:193]
	ds_read_b128 v[162:165], v213 offset:6144
	v_mfma_f32_16x16x32_f16 v[186:189], v[166:169], v[150:153], v[186:189]
	ds_read_b128 v[166:169], v213 offset:7168
	ds_read_b128 v[150:153], v240 offset:768
	s_waitcnt lgkmcnt(7)
	v_mfma_f32_16x16x32_f16 v[182:185], a[8:11], v[138:141], v[182:185]
	v_mfma_f32_16x16x32_f16 v[178:181], a[0:3], v[138:141], v[178:181]
	v_mfma_f32_16x16x32_f16 v[174:177], a[4:7], v[138:141], v[174:177]
	v_mfma_f32_16x16x32_f16 v[170:173], a[32:35], v[138:141], v[170:173]
	ds_read_b128 v[138:141], v241 offset:256
	s_waitcnt lgkmcnt(7)
	v_mfma_f32_16x16x32_f16 v[182:185], a[28:31], v[142:145], v[182:185]
	v_exp_f32_e32 v198, v198
	v_mfma_f32_16x16x32_f16 v[178:181], a[36:39], v[142:145], v[178:181]
	v_exp_f32_e32 v199, v199
	v_mfma_f32_16x16x32_f16 v[174:177], a[40:43], v[142:145], v[174:177]
	v_exp_f32_e32 v200, v200
	v_mfma_f32_16x16x32_f16 v[170:173], a[44:47], v[142:145], v[170:173]
	ds_read_b128 v[142:145], v240 offset:512
	v_exp_f32_e32 v201, v201
	s_waitcnt lgkmcnt(7)
	v_mfma_f32_16x16x32_f16 v[182:185], a[136:139], v[146:149], v[182:185]
	v_exp_f32_e32 v194, v194
	v_mfma_f32_16x16x32_f16 v[178:181], a[128:131], v[146:149], v[178:181]
	v_exp_f32_e32 v195, v195
	v_mfma_f32_16x16x32_f16 v[174:177], a[132:135], v[146:149], v[174:177]
	v_exp_f32_e32 v196, v196
	v_mfma_f32_16x16x32_f16 v[170:173], a[152:155], v[146:149], v[170:173]
	ds_read_b128 v[146:149], v241 offset:512
	v_exp_f32_e32 v197, v197
	s_waitcnt lgkmcnt(3)
	v_mfma_f32_16x16x32_f16 v[182:185], v[154:157], v[150:153], v[182:185]
	ds_read_b128 v[154:157], v213 offset:12288
	v_exp_f32_e32 v190, v190
	v_mfma_f32_16x16x32_f16 v[178:181], v[158:161], v[150:153], v[178:181]
	ds_read_b128 v[158:161], v213 offset:13312
	v_exp_f32_e32 v191, v191
	v_mfma_f32_16x16x32_f16 v[174:177], v[162:165], v[150:153], v[174:177]
	ds_read_b128 v[162:165], v213 offset:14336
	v_exp_f32_e32 v192, v192
	v_mfma_f32_16x16x32_f16 v[170:173], v[166:169], v[150:153], v[170:173]
	ds_read_b128 v[166:169], v213 offset:15360
	ds_read_b128 v[150:153], v241 offset:768
	v_exp_f32_e32 v193, v193
	s_waitcnt lgkmcnt(7)
	v_mfma_f32_16x16x32_f16 v[182:185], a[172:175], v[138:141], v[182:185]
	v_exp_f32_e32 v186, v186
	v_mfma_f32_16x16x32_f16 v[178:181], a[156:159], v[138:141], v[178:181]
	v_exp_f32_e32 v187, v187
	v_mfma_f32_16x16x32_f16 v[174:177], a[160:163], v[138:141], v[174:177]
	v_exp_f32_e32 v188, v188
	v_mfma_f32_16x16x32_f16 v[170:173], a[164:167], v[138:141], v[170:173]
	ds_read_b128 v[138:141], v242 offset:0
	v_exp_f32_e32 v189, v189
	s_waitcnt lgkmcnt(7)
	v_mfma_f32_16x16x32_f16 v[182:185], v[50:53], v[142:145], v[182:185]
	v_add_f32_e32 v198, 1.0, v198
	v_add_f32_e32 v199, 1.0, v199
	v_mfma_f32_16x16x32_f16 v[178:181], v[26:29], v[142:145], v[178:181]
	v_add_f32_e32 v200, 1.0, v200
	v_add_f32_e32 v201, 1.0, v201
	v_mfma_f32_16x16x32_f16 v[174:177], v[30:33], v[142:145], v[174:177]
	v_add_f32_e32 v194, 1.0, v194
	v_add_f32_e32 v195, 1.0, v195
	v_mfma_f32_16x16x32_f16 v[170:173], v[34:37], v[142:145], v[170:173]
	ds_read_b128 v[142:145], v243 offset:0
	v_add_f32_e32 v196, 1.0, v196
	v_add_f32_e32 v197, 1.0, v197
	s_waitcnt lgkmcnt(7)
	v_mfma_f32_16x16x32_f16 v[182:185], v[70:73], v[146:149], v[182:185]
	v_add_f32_e32 v190, 1.0, v190
	v_add_f32_e32 v191, 1.0, v191
	v_mfma_f32_16x16x32_f16 v[178:181], v[38:41], v[146:149], v[178:181]
	v_add_f32_e32 v192, 1.0, v192
	v_add_f32_e32 v193, 1.0, v193
	v_mfma_f32_16x16x32_f16 v[174:177], v[42:45], v[146:149], v[174:177]
	v_add_f32_e32 v186, 1.0, v186
	v_add_f32_e32 v187, 1.0, v187
	v_mfma_f32_16x16x32_f16 v[170:173], v[46:49], v[146:149], v[170:173]
	ds_read_b128 v[146:149], v242 offset:256
	v_add_f32_e32 v188, 1.0, v188
	v_add_f32_e32 v189, 1.0, v189
	s_waitcnt lgkmcnt(3)
	v_mfma_f32_16x16x32_f16 v[182:185], v[154:157], v[150:153], v[182:185]
	ds_read_b128 v[154:157], v213 offset:20480
	v_rcp_f32_e32 v198, v198
	v_mfma_f32_16x16x32_f16 v[178:181], v[158:161], v[150:153], v[178:181]
	ds_read_b128 v[158:161], v213 offset:21504
	v_rcp_f32_e32 v199, v199
	v_mfma_f32_16x16x32_f16 v[174:177], v[162:165], v[150:153], v[174:177]
	ds_read_b128 v[162:165], v213 offset:22528
	v_rcp_f32_e32 v200, v200
	v_mfma_f32_16x16x32_f16 v[170:173], v[166:169], v[150:153], v[170:173]
	ds_read_b128 v[166:169], v213 offset:23552
	ds_read_b128 v[150:153], v242 offset:768
	v_rcp_f32_e32 v201, v201
	s_waitcnt lgkmcnt(7)
	v_mfma_f32_16x16x32_f16 v[182:185], a[72:75], v[138:141], v[182:185]
	v_rcp_f32_e32 v194, v194
	v_mfma_f32_16x16x32_f16 v[178:181], a[64:67], v[138:141], v[178:181]
	v_rcp_f32_e32 v195, v195
	v_mfma_f32_16x16x32_f16 v[174:177], a[68:71], v[138:141], v[174:177]
	v_rcp_f32_e32 v196, v196
	v_mfma_f32_16x16x32_f16 v[170:173], a[96:99], v[138:141], v[170:173]
	ds_read_b128 v[138:141], v243 offset:256
	v_rcp_f32_e32 v197, v197
	s_waitcnt lgkmcnt(7)
	v_mfma_f32_16x16x32_f16 v[182:185], a[92:95], v[142:145], v[182:185]
	v_rcp_f32_e32 v190, v190
	v_mfma_f32_16x16x32_f16 v[178:181], a[100:103], v[142:145], v[178:181]
	v_rcp_f32_e32 v191, v191
	v_mfma_f32_16x16x32_f16 v[174:177], a[104:107], v[142:145], v[174:177]
	v_rcp_f32_e32 v192, v192
	v_mfma_f32_16x16x32_f16 v[170:173], a[108:111], v[142:145], v[170:173]
	ds_read_b128 v[142:145], v242 offset:512
	v_rcp_f32_e32 v193, v193
	s_waitcnt lgkmcnt(7)
	v_mfma_f32_16x16x32_f16 v[182:185], a[208:211], v[146:149], v[182:185]
	v_rcp_f32_e32 v186, v186
	v_mfma_f32_16x16x32_f16 v[178:181], a[224:227], v[146:149], v[178:181]
	v_rcp_f32_e32 v187, v187
	v_mfma_f32_16x16x32_f16 v[174:177], a[228:231], v[146:149], v[174:177]
	v_rcp_f32_e32 v188, v188
	v_mfma_f32_16x16x32_f16 v[170:173], a[240:243], v[146:149], v[170:173]
	ds_read_b128 v[146:149], v243 offset:512
	v_rcp_f32_e32 v189, v189
	s_waitcnt lgkmcnt(3)
	v_mfma_f32_16x16x32_f16 v[182:185], v[154:157], v[150:153], v[182:185]
	ds_read_b128 v[154:157], v213 offset:28672
	v_fma_f32 v198, v198, -2.0, 1.0
	v_fma_f32 v199, v199, -2.0, 1.0
	v_mfma_f32_16x16x32_f16 v[178:181], v[158:161], v[150:153], v[178:181]
	ds_read_b128 v[158:161], v213 offset:29696
	v_fma_f32 v200, v200, -2.0, 1.0
	v_fma_f32 v201, v201, -2.0, 1.0
	v_mfma_f32_16x16x32_f16 v[174:177], v[162:165], v[150:153], v[174:177]
	ds_read_b128 v[162:165], v213 offset:30720
	v_fma_f32 v194, v194, -2.0, 1.0
	v_fma_f32 v195, v195, -2.0, 1.0
	v_mfma_f32_16x16x32_f16 v[170:173], v[166:169], v[150:153], v[170:173]
	ds_read_b128 v[166:169], v213 offset:31744
	ds_read_b128 v[150:153], v243 offset:768
	v_fma_f32 v196, v196, -2.0, 1.0
	v_fma_f32 v197, v197, -2.0, 1.0
	s_waitcnt lgkmcnt(7)
	v_mfma_f32_16x16x32_f16 v[182:185], a[236:239], v[138:141], v[182:185]
	v_fma_f32 v190, v190, -2.0, 1.0
	v_fma_f32 v191, v191, -2.0, 1.0
	v_mfma_f32_16x16x32_f16 v[178:181], a[244:247], v[138:141], v[178:181]
	v_fma_f32 v192, v192, -2.0, 1.0
	v_fma_f32 v193, v193, -2.0, 1.0
	v_mfma_f32_16x16x32_f16 v[174:177], v[2:5], v[138:141], v[174:177]
	v_fma_f32 v186, v186, -2.0, 1.0
	v_fma_f32 v187, v187, -2.0, 1.0
	v_mfma_f32_16x16x32_f16 v[170:173], v[6:9], v[138:141], v[170:173]
	v_fma_f32 v188, v188, -2.0, 1.0
	v_fma_f32 v189, v189, -2.0, 1.0
	s_waitcnt lgkmcnt(6)
	v_mfma_f32_16x16x32_f16 v[182:185], v[90:93], v[142:145], v[182:185]
	v_cvt_pk_f16_f32 v198, v198, v199
	v_cvt_pk_f16_f32 v199, v200, v201
	v_mfma_f32_16x16x32_f16 v[178:181], v[114:117], v[142:145], v[178:181]
	v_cvt_pk_f16_f32 v194, v194, v195
	v_cvt_pk_f16_f32 v195, v196, v197
	v_mfma_f32_16x16x32_f16 v[174:177], v[118:121], v[142:145], v[174:177]
	v_cvt_pk_f16_f32 v190, v190, v191
	v_cvt_pk_f16_f32 v191, v192, v193
	v_mfma_f32_16x16x32_f16 v[170:173], v[122:125], v[142:145], v[170:173]
	v_cvt_pk_f16_f32 v186, v186, v187
	v_cvt_pk_f16_f32 v187, v188, v189
	s_waitcnt lgkmcnt(5)
	v_mfma_f32_16x16x32_f16 v[182:185], v[110:113], v[146:149], v[182:185]
	v_add_u32_e32 v244, s5, v217
	v_mfma_f32_16x16x32_f16 v[178:181], v[126:129], v[146:149], v[178:181]
	ds_write_b64 v244, v[198:199]
	v_mfma_f32_16x16x32_f16 v[174:177], v[130:133], v[146:149], v[174:177]
	v_add_u32_e32 v245, s5, v215
	v_mfma_f32_16x16x32_f16 v[170:173], v[134:137], v[146:149], v[170:173]
	ds_write_b64 v245, v[194:195]
	s_waitcnt lgkmcnt(2)
	v_mfma_f32_16x16x32_f16 v[182:185], v[154:157], v[150:153], v[182:185]
	v_add_u32_e32 v246, s5, v211
	v_mfma_f32_16x16x32_f16 v[178:181], v[158:161], v[150:153], v[178:181]
	ds_write_b64 v246, v[190:191]
	v_mfma_f32_16x16x32_f16 v[174:177], v[162:165], v[150:153], v[174:177]
	v_add_u32_e32 v247, s5, v212
	v_mfma_f32_16x16x32_f16 v[170:173], v[166:169], v[150:153], v[170:173]
	ds_write_b64 v247, v[186:187]
	ds_read_b128 v[154:157], v213 offset:0
	ds_read_b128 v[158:161], v213 offset:1024
	ds_read_b128 v[162:165], v213 offset:2048
	ds_read_b128 v[166:169], v213 offset:3072
	s_waitcnt vmcnt(2)
	v_cvt_f32_f16_e32 v198, v224
	v_cvt_f32_f16_sdwa v199, v224 dst_sel:DWORD dst_unused:UNUSED_PAD src0_sel:WORD_1
	v_cvt_f32_f16_e32 v200, v225
	v_cvt_f32_f16_sdwa v201, v225 dst_sel:DWORD dst_unused:UNUSED_PAD src0_sel:WORD_1
	v_cvt_f32_f16_e32 v194, v226
	v_cvt_f32_f16_sdwa v195, v226 dst_sel:DWORD dst_unused:UNUSED_PAD src0_sel:WORD_1
	v_cvt_f32_f16_e32 v196, v227
	v_cvt_f32_f16_sdwa v197, v227 dst_sel:DWORD dst_unused:UNUSED_PAD src0_sel:WORD_1
	v_cvt_f32_f16_e32 v190, v228
	v_cvt_f32_f16_sdwa v191, v228 dst_sel:DWORD dst_unused:UNUSED_PAD src0_sel:WORD_1
	v_cvt_f32_f16_e32 v192, v229
	v_cvt_f32_f16_sdwa v193, v229 dst_sel:DWORD dst_unused:UNUSED_PAD src0_sel:WORD_1
	v_cvt_f32_f16_e32 v186, v230
	v_cvt_f32_f16_sdwa v187, v230 dst_sel:DWORD dst_unused:UNUSED_PAD src0_sel:WORD_1
	v_cvt_f32_f16_e32 v188, v231
	v_cvt_f32_f16_sdwa v189, v231 dst_sel:DWORD dst_unused:UNUSED_PAD src0_sel:WORD_1
	s_addk_i32 s3, 0x4000
	v_lshl_add_u64 v[208:209], v[208:209], 0, s[0:1]
	s_cmp_eq_u32 s3, 0x44000
	s_waitcnt lgkmcnt(0)
	s_barrier
	s_cbranch_scc0 .Lrnn_top
	s_and_b32 s5, s3, 0x4000
	s_xor_b32 s5, s5, 0x4000
	s_add_i32 s5, s5, 0x20000
	s_nop 7
	v_exp_f32_e32 v182, v182
	v_exp_f32_e32 v183, v183
	v_exp_f32_e32 v184, v184
	v_exp_f32_e32 v185, v185
	v_exp_f32_e32 v178, v178
	v_exp_f32_e32 v179, v179
	v_exp_f32_e32 v180, v180
	v_exp_f32_e32 v181, v181
	v_exp_f32_e32 v174, v174
	v_exp_f32_e32 v175, v175
	v_exp_f32_e32 v176, v176
	v_exp_f32_e32 v177, v177
	v_exp_f32_e32 v170, v170
	v_exp_f32_e32 v171, v171
	v_exp_f32_e32 v172, v172
	v_exp_f32_e32 v173, v173
	v_add_f32_e32 v182, 1.0, v182
	v_add_f32_e32 v183, 1.0, v183
	v_add_f32_e32 v184, 1.0, v184
	v_add_f32_e32 v185, 1.0, v185
	v_add_f32_e32 v178, 1.0, v178
	v_add_f32_e32 v179, 1.0, v179
	v_add_f32_e32 v180, 1.0, v180
	v_add_f32_e32 v181, 1.0, v181
	v_add_f32_e32 v174, 1.0, v174
	v_add_f32_e32 v175, 1.0, v175
	v_add_f32_e32 v176, 1.0, v176
	v_add_f32_e32 v177, 1.0, v177
	v_add_f32_e32 v170, 1.0, v170
	v_add_f32_e32 v171, 1.0, v171
	v_add_f32_e32 v172, 1.0, v172
	v_add_f32_e32 v173, 1.0, v173
	v_rcp_f32_e32 v182, v182
	v_rcp_f32_e32 v183, v183
	v_rcp_f32_e32 v184, v184
	v_rcp_f32_e32 v185, v185
	v_rcp_f32_e32 v178, v178
	v_rcp_f32_e32 v179, v179
	v_rcp_f32_e32 v180, v180
	v_rcp_f32_e32 v181, v181
	v_rcp_f32_e32 v174, v174
	v_rcp_f32_e32 v175, v175
	v_rcp_f32_e32 v176, v176
	v_rcp_f32_e32 v177, v177
	v_rcp_f32_e32 v170, v170
	v_rcp_f32_e32 v171, v171
	v_rcp_f32_e32 v172, v172
	v_rcp_f32_e32 v173, v173
	v_fma_f32 v182, v182, -2.0, 1.0
	v_fma_f32 v183, v183, -2.0, 1.0
	v_fma_f32 v184, v184, -2.0, 1.0
	v_fma_f32 v185, v185, -2.0, 1.0
	v_fma_f32 v178, v178, -2.0, 1.0
	v_fma_f32 v179, v179, -2.0, 1.0
	v_fma_f32 v180, v180, -2.0, 1.0
	v_fma_f32 v181, v181, -2.0, 1.0
	v_fma_f32 v174, v174, -2.0, 1.0
	v_fma_f32 v175, v175, -2.0, 1.0
	v_fma_f32 v176, v176, -2.0, 1.0
	v_fma_f32 v177, v177, -2.0, 1.0
	v_fma_f32 v170, v170, -2.0, 1.0
	v_fma_f32 v171, v171, -2.0, 1.0
	v_fma_f32 v172, v172, -2.0, 1.0
	v_fma_f32 v173, v173, -2.0, 1.0
	v_cvt_pk_f16_f32 v182, v182, v183
	v_cvt_pk_f16_f32 v183, v184, v185
	v_cvt_pk_f16_f32 v178, v178, v179
	v_cvt_pk_f16_f32 v179, v180, v181
	v_cvt_pk_f16_f32 v174, v174, v175
	v_cvt_pk_f16_f32 v175, v176, v177
	v_cvt_pk_f16_f32 v170, v170, v171
	v_cvt_pk_f16_f32 v171, v172, v173
	v_add_u32_e32 v244, s5, v210
	ds_write_b64 v244, v[182:183]
	v_add_u32_e32 v245, s5, v1
	ds_write_b64 v245, v[178:179]
	v_add_u32_e32 v246, s5, v216
	ds_write_b64 v246, v[174:175]
	v_add_u32_e32 v247, s5, v214
	ds_write_b64 v247, v[170:171]
	s_waitcnt lgkmcnt(0)
